# norm+route: router matrix staged once per WG in LDS (chunk-permuted image), lane-contiguous ds_read_b128 replace 64-line global loads
# speedup vs baseline: 1.0241x; 1.0083x over previous
.LBB0_2066:
	s_or_b64 exec, exec, s[4:5]
	s_lshl_b32 s27, s24, 5
	s_add_i32 s27, s27, s76
	s_add_u32 s29, s22, 0x3df80000
	s_addc_u32 s30, s23, 0
	s_add_u32 s14, s22, 0x8000
	s_addc_u32 s15, s23, 0
	s_add_u32 s31, s22, 0x460000
	s_addc_u32 s33, s23, 0
	s_add_u32 s35, s22, 0x470000
	v_ashrrev_i32_e32 v9, 31, v8
	s_addc_u32 s36, s23, 0
	v_lshlrev_b64 v[2:3], 4, v[8:9]
	s_add_u32 s37, s22, 0x480000
	v_lshl_add_u64 v[22:23], s[6:7], 0, v[2:3]
	s_addc_u32 s38, s23, 0
	v_readlane_b32 s0, v254, 9
	v_readlane_b32 s6, v254, 45
	v_readlane_b32 s1, v254, 10
	s_add_u32 s0, s0, s6
	v_readlane_b32 s6, v254, 46
	s_addc_u32 s1, s1, s6
	v_lshl_add_u64 v[2:3], s[0:1], 0, v[2:3]
	s_mov_b64 s[0:1], 0x2bc80400
	v_lshl_add_u64 v[24:25], v[2:3], 0, s[0:1]
	v_mov_b32_e32 v2, v1
	v_mov_b32_e32 v3, v1
	v_mov_b32_e32 v4, v1
	v_mov_b32_e32 v5, v1
	v_mov_b32_e32 v6, v1
	v_mov_b32_e32 v7, v1
	v_lshlrev_b32_e32 v46, 2, v8
	v_cmp_eq_u32_e64 s[4:5], 0, v8
	v_lshl_add_u32 v49, v8, 4, 0
	v_mov_b32_e32 v0, v1
	v_lshlrev_b64 v[26:27], 2, v[8:9]
	v_mov_b64_e32 v[8:9], v[6:7]
	v_xor_b32_e32 v47, 64, v46
	v_xor_b32_e32 v48, 0x80, v46
	s_mov_b32 s28, 0
	v_mov_b32_e32 v50, 0x358637bd
	s_mov_b32 s39, 0xf800000
	v_mov_b32_e32 v51, 0x260
	s_mov_b32 s40, 0xc3e00000
	s_mov_b64 s[20:21], 0x800
	v_mov_b32_e32 v52, 0x43e00000
	v_mov_b32_e32 v53, 1
	s_mov_b32 s22, s27
	v_mov_b64_e32 v[6:7], v[4:5]
	v_mov_b64_e32 v[4:5], v[2:3]
	v_mov_b64_e32 v[2:3], v[0:1]
	v_lshrrev_b32_e32 v200, 2, v46
	v_lshl_add_u32 v200, s76, 6, v200
	v_lshlrev_b32_e32 v201, 4, v200
	global_load_dwordx4 v[204:207], v201, s[18:19]
	v_add_u32_e32 v202, 0x2000, v201
	global_load_dwordx4 v[208:211], v202, s[18:19]
	v_add_u32_e32 v202, 0x4000, v201
	global_load_dwordx4 v[212:215], v202, s[18:19]
	v_add_u32_e32 v202, 0x6000, v201
	global_load_dwordx4 v[216:219], v202, s[18:19]
	v_add_u32_e32 v202, 0x8000, v201
	global_load_dwordx4 v[220:223], v202, s[18:19]
	v_add_u32_e32 v202, 0xa000, v201
	global_load_dwordx4 v[224:227], v202, s[18:19]
	v_add_u32_e32 v202, 0xc000, v201
	global_load_dwordx4 v[228:231], v202, s[18:19]
	v_add_u32_e32 v202, 0xe000, v201
	global_load_dwordx4 v[232:235], v202, s[18:19]
	v_and_b32_e32 v202, 7, v200
	v_lshrrev_b32_e32 v203, 3, v200
	v_mul_u32_u24_e32 v202, 0x2020, v202
	v_lshl_add_u32 v203, v203, 4, v202
	v_add_u32_e32 v150, 0x4000, v49
	s_waitcnt vmcnt(7)
	ds_write_b128 v203, v[204:207] offset:16384
	s_waitcnt vmcnt(6)
	ds_write_b128 v203, v[208:211] offset:17408
	s_waitcnt vmcnt(5)
	ds_write_b128 v203, v[212:215] offset:18432
	s_waitcnt vmcnt(4)
	ds_write_b128 v203, v[216:219] offset:19456
	s_waitcnt vmcnt(3)
	ds_write_b128 v203, v[220:223] offset:20480
	s_waitcnt vmcnt(2)
	ds_write_b128 v203, v[224:227] offset:21504
	s_waitcnt vmcnt(1)
	ds_write_b128 v203, v[228:231] offset:22528
	s_waitcnt vmcnt(0)
	ds_write_b128 v203, v[232:235] offset:23552
	s_waitcnt lgkmcnt(0)
	s_barrier
	s_branch .LBB0_2068

.LBB0_2069:
	v_lshl_add_u32 v151, s25, 2, v150
	v_add_u32_e32 v44, s25, v46
	v_ashrrev_i32_e32 v45, 31, v44
	v_lshl_add_u64 v[66:67], v[44:45], 2, s[16:17]
	ds_read_b128 v[10:13], v0
	ds_read_b128 v[14:17], v0 offset:1024
	ds_read_b128 v[54:57], v0 offset:8192
	ds_read_b128 v[58:61], v0 offset:9216
	global_load_dwordx4 v[62:65], v[32:33], off offset:-1024
	global_load_dwordx4 v[18:21], v[32:33], off
	v_add_u32_e32 v76, 0x100, v44
	global_load_dwordx4 v[66:69], v[66:67], off
	v_ashrrev_i32_e32 v77, 31, v76
	v_lshl_add_u64 v[90:91], v[76:77], 2, s[16:17]
	ds_read_b128 v[70:73], v151 offset:8224
	ds_read_b128 v[74:77], v151 offset:0
	global_load_dwordx4 v[78:81], v[90:91], off
	ds_read_b128 v[82:85], v151 offset:41120
	ds_read_b128 v[86:89], v151 offset:57568
	ds_read_b128 v[90:93], v151 offset:9248
	ds_read_b128 v[94:97], v151 offset:42144
	ds_read_b128 v[98:101], v151 offset:58592
	ds_read_b128 v[102:105], v151 offset:16448
	ds_read_b128 v[106:109], v151 offset:24672
	ds_read_b128 v[110:113], v151 offset:32896
	ds_read_b128 v[114:117], v151 offset:1024
	s_waitcnt lgkmcnt(14)
	ds_read_b128 v[118:121], v151 offset:33920
	s_waitcnt lgkmcnt(13)
	v_add_f32_e32 v36, 1.0, v54
	ds_read_b128 v[122:125], v151 offset:49344
	v_add_f32_e32 v45, 1.0, v55
	v_pk_add_f32 v[134:135], v[56:57], 1.0 op_sel_hi:[1,0]
	ds_read_b128 v[54:57], v151 offset:25696
	s_waitcnt lgkmcnt(14)
	ds_read_b128 v[126:129], v151 offset:17472
	s_waitcnt lgkmcnt(14)
	ds_read_b128 v[130:133], v151 offset:50368
	v_mov_b32_e32 v43, v11
	v_mov_b32_e32 v136, v14
	s_waitcnt lgkmcnt(15)
	v_pk_add_f32 v[60:61], v[60:61], 1.0 op_sel_hi:[1,0]
	v_mov_b32_e32 v142, 0
	v_add_f32_e32 v59, 1.0, v59
	s_add_i32 s23, s12, -1
	s_cmp_eq_u32 s23, 0
	s_cselect_b64 vcc, -1, 0
	s_cmp_eq_u32 s23, 1
	v_mov_b32_e32 v143, 0
	s_cselect_b64 s[6:7], -1, 0
	s_cmp_eq_u32 s23, 2
	s_cselect_b64 s[8:9], -1, 0
	s_cmp_eq_u32 s23, 3
	s_cselect_b64 s[10:11], -1, 0
	s_cmp_eq_u32 s23, 4
	v_lshl_add_u64 v[32:33], v[32:33], 0, s[20:21]
	v_add_u32_e32 v0, 0x800, v0
	s_waitcnt vmcnt(3)
	v_mul_f32_e32 v11, v37, v62
	v_pk_mul_f32 v[64:65], v[38:39], v[64:65]
	v_mov_b32_e32 v139, v63
	v_pk_mul_f32 v[62:63], v[36:37], v[62:63]
	s_waitcnt vmcnt(2)
	v_mul_f32_e32 v14, v37, v18
	v_pk_mul_f32 v[20:21], v[38:39], v[20:21]
	v_mov_b32_e32 v141, v19
	s_waitcnt vmcnt(1)
	v_mul_f32_e32 v138, v66, v11
	v_mov_b32_e32 v11, v67
	v_pk_mul_f32 v[64:65], v[68:69], v[64:65]
	v_pk_mul_f32 v[62:63], v[66:67], v[62:63]
	v_pk_fma_f32 v[10:11], v[36:37], v[138:139], v[10:11]
	v_pk_fma_f32 v[12:13], v[134:135], v[64:65], v[12:13]
	v_mov_b32_e32 v62, v10
	v_add_f32_e32 v36, 1.0, v58
	v_pk_mul_f32 v[18:19], v[36:37], v[18:19]
	s_waitcnt vmcnt(1) lgkmcnt(15)
	v_mov_b32_e32 v44, v73
	s_waitcnt vmcnt(1) lgkmcnt(14)
	v_pk_fma_f32 v[40:41], v[74:75], v[10:11], v[40:41] op_sel_hi:[1,0,1]
	s_waitcnt vmcnt(0) lgkmcnt(14)
	v_mul_f32_e32 v140, v78, v14
	v_pk_mul_f32 v[20:21], v[80:81], v[20:21]
	v_cvt_pk_bf16_f32 v14, v12, v13
	v_mov_b32_e32 v137, v79
	s_waitcnt vmcnt(0) lgkmcnt(13)
	v_mov_b32_e32 v66, v85
	s_waitcnt vmcnt(0) lgkmcnt(12)
	v_mov_b32_e32 v67, v89
	v_pk_fma_f32 v[16:17], v[60:61], v[20:21], v[16:17]
	v_pk_fma_f32 v[42:43], v[44:45], v[62:63], v[42:43]
	v_lshlrev_b32_e32 v29, 16, v14
	v_fmac_f32_e32 v28, v72, v10
	v_pk_fma_f32 v[34:35], v[76:77], v[10:11], v[34:35] op_sel_hi:[1,0,1]
	v_pk_fma_f32 v[30:31], v[70:71], v[10:11], v[30:31] op_sel_hi:[1,0,1]
	v_pk_fma_f32 v[70:71], v[36:37], v[140:141], v[136:137]
	s_waitcnt vmcnt(0) lgkmcnt(10)
	v_mov_b32_e32 v20, v97
	s_waitcnt vmcnt(0) lgkmcnt(9)
	v_mov_b32_e32 v21, v101
	v_and_b32_e32 v14, 0xffff0000, v14
	v_pk_mul_f32 v[44:45], v[12:13], v[66:67]
	v_cvt_pk_bf16_f32 v36, v16, v17
	v_cvt_pk_bf16_f32 v66, v10, v43
	s_waitcnt vmcnt(0) lgkmcnt(8)
	v_pk_fma_f32 v[10:11], v[42:43], v[102:103], v[40:41] op_sel:[1,0,0]
	v_mul_f32_e32 v40, 0x41800000, v29
	v_mov_b32_e32 v29, v42
	v_mul_f32_e32 v64, v12, v84
	v_pk_mul_f32 v[20:21], v[16:17], v[20:21]
	v_pk_fma_f32 v[34:35], v[42:43], v[104:105], v[34:35] op_sel:[1,0,0]
	s_waitcnt vmcnt(0) lgkmcnt(7)
	v_pk_fma_f32 v[30:31], v[42:43], v[106:107], v[30:31] op_sel:[1,0,0]
	v_mov_b32_e32 v65, v44
	v_mov_b32_e32 v69, v45
	v_mul_f32_e32 v14, 0x41800000, v14
	v_lshlrev_b32_e32 v41, 16, v36
	v_and_b32_e32 v36, 0xffff0000, v36
	v_lshlrev_b32_e32 v44, 16, v66
	v_and_b32_e32 v45, 0xffff0000, v66
	v_pk_fma_f32 v[28:29], v[42:43], v[108:109], v[28:29] op_sel:[1,0,0]
	v_mul_f32_e32 v68, v13, v88
	v_mov_b32_e32 v61, v20
	v_mov_b32_e32 v63, v21
	s_waitcnt vmcnt(0) lgkmcnt(6)
	v_pk_fma_f32 v[10:11], v[12:13], v[110:111], v[10:11] op_sel_hi:[0,1,1]
	v_pk_fma_f32 v[20:21], v[12:13], v[112:113], v[34:35] op_sel_hi:[0,1,1]
	v_pk_fma_f32 v[30:31], v[12:13], v[82:83], v[30:31] op_sel_hi:[0,1,1]
	v_med3_f32 v34, v14, s40, v52
	v_mul_f32_e32 v14, 0x41800000, v41
	v_mul_f32_e32 v35, 0x41800000, v36
	v_mul_f32_e32 v36, 0x41800000, v44
	v_mul_f32_e32 v41, 0x41800000, v45
	v_pk_add_f32 v[28:29], v[28:29], v[64:65]
	v_pk_mul_f32 v[18:19], v[78:79], v[18:19]
	s_waitcnt vmcnt(0) lgkmcnt(3)
	v_pk_fma_f32 v[10:11], v[12:13], v[122:123], v[10:11] op_sel:[1,0,0]
	v_pk_fma_f32 v[20:21], v[12:13], v[124:125], v[20:21] op_sel:[1,0,0]
	v_pk_fma_f32 v[12:13], v[12:13], v[86:87], v[30:31] op_sel:[1,0,0]
	v_med3_f32 v43, v14, s40, v52
	v_med3_f32 v14, v36, s40, v52
	v_med3_f32 v30, v41, s40, v52
	v_pk_add_f32 v[28:29], v[28:29], v[68:69]
	v_mov_b32_e32 v58, v93
	v_mov_b32_e32 v18, v70
	v_cvt_pk_fp8_f32 v142, v14, v30
	v_mov_b32_e32 v14, v29
	v_pk_fma_f32 v[14:15], v[58:59], v[18:19], v[14:15]
	v_pk_fma_f32 v[20:21], v[116:117], v[70:71], v[20:21] op_sel_hi:[1,0,1]
	v_pk_fma_f32 v[12:13], v[90:91], v[70:71], v[12:13] op_sel_hi:[1,0,1]
	v_cvt_pk_bf16_f32 v30, v70, v15
	v_med3_f32 v40, v40, s40, v52
	s_waitcnt vmcnt(0) lgkmcnt(1)
	v_pk_fma_f32 v[18:19], v[14:15], v[128:129], v[20:21] op_sel:[1,0,0]
	v_pk_fma_f32 v[12:13], v[14:15], v[54:55], v[12:13] op_sel:[1,0,0]
	v_lshlrev_b32_e32 v20, 16, v30
	v_and_b32_e32 v21, 0xffff0000, v30
	v_pk_fma_f32 v[12:13], v[16:17], v[94:95], v[12:13] op_sel_hi:[0,1,1]
	v_cvt_pk_fp8_f32 v142, v40, v34 op_sel:[0,0,1]
	v_mul_f32_e32 v20, 0x41800000, v20
	v_mul_f32_e32 v21, 0x41800000, v21
	v_pk_fma_f32 v[30:31], v[16:17], v[98:99], v[12:13] op_sel:[1,0,0]
	v_med3_f32 v12, v20, s40, v52
	v_med3_f32 v13, v21, s40, v52
	v_cvt_pk_fp8_f32 v143, v12, v13
	v_cndmask_b32_e32 v2, v2, v142, vcc
	s_cselect_b64 vcc, -1, 0
	s_cmp_eq_u32 s23, 5
	v_med3_f32 v44, v35, s40, v52
	v_cndmask_b32_e32 v6, v6, v142, vcc
	s_cselect_b64 vcc, -1, 0
	s_cmp_eq_u32 s23, 6
	v_cndmask_b32_e32 v7, v7, v142, vcc
	s_cselect_b64 vcc, -1, 0
	s_cmp_eq_u32 s23, 7
	v_cvt_pk_fp8_f32 v143, v43, v44 op_sel:[0,0,1]
	v_cndmask_b32_e32 v8, v8, v142, vcc
	s_cselect_b64 vcc, -1, 0
	s_cmp_eq_u32 s12, 7
	v_cndmask_b32_e32 v9, v9, v142, vcc
	s_cselect_b64 vcc, -1, 0
	s_cmp_eq_u32 s12, 6
	v_cndmask_b32_e64 v3, v3, v142, s[6:7]
	s_cselect_b64 s[6:7], -1, 0
	s_cmp_eq_u32 s12, 5
	v_cndmask_b32_e32 v9, v9, v143, vcc
	s_cselect_b64 vcc, -1, 0
	s_cmp_eq_u32 s12, 4
	v_cndmask_b32_e32 v7, v7, v143, vcc
	s_cselect_b64 vcc, -1, 0
	s_cmp_eq_u32 s12, 3
	v_cndmask_b32_e64 v5, v5, v142, s[10:11]
	v_cndmask_b32_e32 v6, v6, v143, vcc
	s_cselect_b64 vcc, -1, 0
	s_cmp_eq_u32 s12, 2
	v_pk_fma_f32 v[10:11], v[114:115], v[70:71], v[10:11] op_sel_hi:[1,0,1]
	v_cndmask_b32_e64 v4, v4, v142, s[8:9]
	v_cndmask_b32_e32 v5, v5, v143, vcc
	s_cselect_b64 vcc, -1, 0
	s_cmp_eq_u32 s12, 1
	v_fmac_f32_e32 v28, v92, v70
	v_pk_fma_f32 v[10:11], v[14:15], v[126:127], v[10:11] op_sel:[1,0,0]
	v_mov_b32_e32 v29, v14
	v_cndmask_b32_e32 v4, v4, v143, vcc
	s_cselect_b64 vcc, -1, 0
	s_cmp_eq_u32 s12, 0
	v_mul_f32_e32 v60, v16, v96
	v_pk_fma_f32 v[10:11], v[16:17], v[118:119], v[10:11] op_sel_hi:[0,1,1]
	v_pk_fma_f32 v[14:15], v[14:15], v[56:57], v[28:29] op_sel:[1,0,0]
	v_cndmask_b32_e32 v3, v3, v143, vcc
	s_cselect_b64 vcc, -1, 0
	s_addk_i32 s25, 0x200
	v_mul_f32_e32 v62, v17, v100
	s_waitcnt vmcnt(0) lgkmcnt(0)
	v_pk_fma_f32 v[40:41], v[16:17], v[130:131], v[10:11] op_sel:[1,0,0]
	v_pk_add_f32 v[10:11], v[14:15], v[60:61]
	s_add_u32 s12, s12, 2
	v_pk_fma_f32 v[18:19], v[16:17], v[120:121], v[18:19] op_sel_hi:[0,1,1]
	v_pk_add_f32 v[28:29], v[10:11], v[62:63]
	s_addc_u32 s13, s13, 0
	v_pk_fma_f32 v[34:35], v[16:17], v[132:133], v[18:19] op_sel:[1,0,0]
	v_mov_b32_e32 v42, v29
	v_cndmask_b32_e64 v8, v8, v143, s[6:7]
	s_cmpk_eq_i32 s25, 0x800
	v_cndmask_b32_e32 v2, v2, v143, vcc
	s_cbranch_scc0 .LBB0_2069
	v_mov_b32_dpp v10, v40 quad_perm:[1,0,3,2] row_mask:0xf bank_mask:0xf bound_ctrl:1
	v_mov_b32_dpp v11, v41 quad_perm:[1,0,3,2] row_mask:0xf bank_mask:0xf bound_ctrl:1
	v_pk_add_f32 v[10:11], v[40:41], v[10:11]
	v_add_f32_dpp v0, v34, v34 quad_perm:[1,0,3,2] row_mask:0xf bank_mask:0xf bound_ctrl:1
	v_add_f32_dpp v15, v35, v35 quad_perm:[1,0,3,2] row_mask:0xf bank_mask:0xf bound_ctrl:1
	v_mov_b32_dpp v12, v10 quad_perm:[2,3,0,1] row_mask:0xf bank_mask:0xf bound_ctrl:1
	v_mov_b32_dpp v13, v11 quad_perm:[2,3,0,1] row_mask:0xf bank_mask:0xf bound_ctrl:1
	v_pk_add_f32 v[10:11], v[10:11], v[12:13]
	v_add_f32_dpp v0, v0, v0 quad_perm:[2,3,0,1] row_mask:0xf bank_mask:0xf bound_ctrl:1
	v_add_f32_dpp v15, v15, v15 quad_perm:[2,3,0,1] row_mask:0xf bank_mask:0xf bound_ctrl:1
	v_mov_b32_dpp v12, v10 row_half_mirror row_mask:0xf bank_mask:0xf bound_ctrl:1
	v_mov_b32_dpp v13, v11 row_half_mirror row_mask:0xf bank_mask:0xf bound_ctrl:1
	v_add_f32_dpp v0, v0, v0 row_half_mirror row_mask:0xf bank_mask:0xf bound_ctrl:1
	v_pk_add_f32 v[10:11], v[10:11], v[12:13]
	v_add_f32_dpp v15, v15, v15 row_half_mirror row_mask:0xf bank_mask:0xf bound_ctrl:1
	v_add_f32_dpp v0, v0, v0 row_mirror row_mask:0xf bank_mask:0xf bound_ctrl:1
	v_mov_b32_dpp v12, v10 row_mirror row_mask:0xf bank_mask:0xf bound_ctrl:1
	v_mov_b32_dpp v13, v11 row_mirror row_mask:0xf bank_mask:0xf bound_ctrl:1
	ds_bpermute_b32 v14, v47, v0
	v_pk_add_f32 v[10:11], v[10:11], v[12:13]
	ds_bpermute_b32 v12, v47, v10
	ds_bpermute_b32 v13, v47, v11
	v_add_f32_dpp v16, v30, v30 quad_perm:[1,0,3,2] row_mask:0xf bank_mask:0xf bound_ctrl:1
	s_waitcnt lgkmcnt(2)
	v_add_f32_e32 v0, v0, v14
	ds_bpermute_b32 v14, v48, v0
	v_add_f32_dpp v15, v15, v15 row_mirror row_mask:0xf bank_mask:0xf bound_ctrl:1
	s_waitcnt lgkmcnt(1)
	v_pk_add_f32 v[10:11], v[10:11], v[12:13]
	v_add_f32_dpp v16, v16, v16 quad_perm:[2,3,0,1] row_mask:0xf bank_mask:0xf bound_ctrl:1
	ds_bpermute_b32 v12, v48, v10
	ds_bpermute_b32 v13, v48, v11
	ds_bpermute_b32 v18, v47, v15
	v_add_f32_dpp v16, v16, v16 row_half_mirror row_mask:0xf bank_mask:0xf bound_ctrl:1
	s_waitcnt lgkmcnt(3)
	v_add_f32_e32 v0, v0, v14
	v_add_f32_dpp v14, v31, v31 quad_perm:[1,0,3,2] row_mask:0xf bank_mask:0xf bound_ctrl:1
	v_add_f32_dpp v19, v16, v16 row_mirror row_mask:0xf bank_mask:0xf bound_ctrl:1
	ds_bpermute_b32 v20, v47, v19
	v_add_f32_dpp v14, v14, v14 quad_perm:[2,3,0,1] row_mask:0xf bank_mask:0xf bound_ctrl:1
	s_waitcnt lgkmcnt(2)
	v_pk_add_f32 v[16:17], v[10:11], v[12:13]
	s_waitcnt lgkmcnt(1)
	v_add_f32_e32 v10, v15, v18
	v_add_f32_dpp v14, v14, v14 row_half_mirror row_mask:0xf bank_mask:0xf bound_ctrl:1
	v_add_f32_dpp v18, v28, v28 quad_perm:[1,0,3,2] row_mask:0xf bank_mask:0xf bound_ctrl:1
	ds_bpermute_b32 v11, v48, v10
	v_add_f32_dpp v14, v14, v14 row_mirror row_mask:0xf bank_mask:0xf bound_ctrl:1
	v_add_f32_dpp v18, v18, v18 quad_perm:[2,3,0,1] row_mask:0xf bank_mask:0xf bound_ctrl:1
	s_waitcnt lgkmcnt(1)
	v_add_f32_e32 v12, v19, v20
	ds_bpermute_b32 v15, v47, v14
	v_add_f32_dpp v18, v18, v18 row_half_mirror row_mask:0xf bank_mask:0xf bound_ctrl:1
	v_add_f32_dpp v20, v29, v29 quad_perm:[1,0,3,2] row_mask:0xf bank_mask:0xf bound_ctrl:1
	ds_bpermute_b32 v13, v48, v12
	v_add_f32_dpp v18, v18, v18 row_mirror row_mask:0xf bank_mask:0xf bound_ctrl:1
	v_add_f32_dpp v20, v20, v20 quad_perm:[2,3,0,1] row_mask:0xf bank_mask:0xf bound_ctrl:1
	ds_bpermute_b32 v19, v47, v18
	v_cmp_gt_f32_e64 s[6:7], v17, v16
	v_add_f32_dpp v20, v20, v20 row_half_mirror row_mask:0xf bank_mask:0xf bound_ctrl:1
	s_waitcnt lgkmcnt(2)
	v_add_f32_e32 v14, v14, v15
	v_add_f32_e32 v11, v10, v11
	v_add_f32_dpp v20, v20, v20 row_mirror row_mask:0xf bank_mask:0xf bound_ctrl:1
	ds_bpermute_b32 v21, v47, v20
	v_cndmask_b32_e64 v10, v16, v17, s[6:7]
	ds_bpermute_b32 v15, v48, v14
	v_cmp_gt_f32_e32 vcc, v0, v10
	s_waitcnt lgkmcnt(2)
	v_add_f32_e32 v18, v18, v19
	v_add_f32_e32 v28, v12, v13
	v_cndmask_b32_e64 v12, 0, 1, s[6:7]
	v_cndmask_b32_e32 v10, v10, v0, vcc
	ds_bpermute_b32 v19, v48, v18
	v_cndmask_b32_e64 v12, v12, 2, vcc
	v_cmp_gt_f32_e32 vcc, v11, v10
	s_waitcnt lgkmcnt(2)
	v_add_f32_e32 v20, v20, v21
	ds_bpermute_b32 v21, v48, v20
	v_cndmask_b32_e32 v10, v10, v11, vcc
	v_cndmask_b32_e64 v12, v12, 3, vcc
	v_cmp_gt_f32_e32 vcc, v28, v10
	s_waitcnt lgkmcnt(2)
	v_add_f32_e32 v15, v14, v15
	s_waitcnt lgkmcnt(1)
	v_add_f32_e32 v18, v18, v19
	v_cndmask_b32_e32 v10, v10, v28, vcc
	v_cndmask_b32_e64 v12, v12, 4, vcc
	v_cmp_gt_f32_e32 vcc, v15, v10
	s_waitcnt lgkmcnt(0)
	v_add_f32_e32 v13, v20, v21
	v_cndmask_b32_e32 v10, v10, v15, vcc
	v_cmp_gt_f32_e64 s[8:9], v18, v10
	v_cndmask_b32_e64 v12, v12, 5, vcc
	s_nop 0
	v_cndmask_b32_e64 v14, v10, v18, s[8:9]
	v_cndmask_b32_e64 v10, v12, 6, s[8:9]
	v_cmp_ngt_f32_e32 vcc, v13, v14
	v_mov_b32_e32 v12, 0
	s_nop 0
	v_cndmask_b32_e32 v10, 7, v10, vcc
	v_cmp_eq_u32_e64 s[10:11], 0, v10
	v_cmp_ne_u32_e64 s[12:13], 1, v10
	s_or_b64 s[0:1], s[10:11], s[6:7]
	s_and_b64 s[6:7], s[12:13], s[0:1]
	v_cndmask_b32_e64 v16, v16, v17, s[6:7]
	v_cndmask_b32_e64 v19, 0, 1, s[6:7]
	v_cmp_gt_f32_e64 s[6:7], v0, v16
	s_nop 1
	v_cndmask_b32_e64 v17, v19, 2, s[6:7]
	v_cndmask_b32_e64 v0, v16, v0, s[6:7]
	v_cmp_eq_u32_e64 s[6:7], 2, v10
	s_nop 1
	v_cndmask_b32_e64 v16, v0, v16, s[6:7]
	v_cndmask_b32_e64 v19, v17, v19, s[6:7]
	v_cmp_gt_f32_e64 s[6:7], v11, v16
	s_nop 1
	v_cndmask_b32_e64 v19, v19, 3, s[6:7]
	v_cndmask_b32_e64 v11, v16, v11, s[6:7]
	v_cmp_eq_u32_e64 s[6:7], 3, v10
	s_nop 1
	v_cndmask_b32_e64 v0, v11, v0, s[6:7]
	v_cndmask_b32_e64 v16, v19, v17, s[6:7]
	v_cmp_gt_f32_e64 s[6:7], v28, v0
	s_nop 1
	v_cndmask_b32_e64 v16, v16, 4, s[6:7]
	v_cndmask_b32_e64 v0, v0, v28, s[6:7]
	v_cmp_eq_u32_e64 s[6:7], 4, v10
	s_nop 1
	v_cndmask_b32_e64 v11, v0, v11, s[6:7]
	v_cndmask_b32_e64 v17, v16, v19, s[6:7]
	v_cmp_gt_f32_e64 s[6:7], v15, v11
	s_nop 1
	v_cndmask_b32_e64 v17, v17, 5, s[6:7]
	v_cndmask_b32_e64 v11, v11, v15, s[6:7]
	v_cmp_eq_u32_e64 s[6:7], 5, v10
	s_nop 1
	v_cndmask_b32_e64 v0, v11, v0, s[6:7]
	v_cndmask_b32_e64 v15, v17, v16, s[6:7]
	v_cmp_gt_f32_e64 s[6:7], v18, v0
	s_nop 1
	v_cndmask_b32_e64 v11, v15, 6, s[6:7]
	v_cndmask_b32_e64 v16, v0, v18, s[6:7]
	s_and_b64 s[6:7], s[8:9], vcc
	v_cndmask_b32_e64 v17, v11, v15, s[6:7]
	v_cndmask_b32_e64 v15, v16, v0, s[6:7]
	v_cmp_gt_f32_e64 s[6:7], v13, v15
	s_nop 1
	v_cndmask_b32_e64 v0, v17, 7, s[6:7]
	v_cndmask_b32_e32 v11, v11, v0, vcc
	v_mov_b32_e32 v0, 0
	s_and_saveexec_b64 s[8:9], s[4:5]
	s_cbranch_execz .LBB0_2067
	v_lshlrev_b32_e32 v0, 6, v10
	v_lshl_add_u64 v[16:17], v[0:1], 2, s[14:15]
	v_lshlrev_b32_e32 v0, 6, v11
	global_atomic_add v12, v[16:17], v53, off sc0
	v_lshl_add_u64 v[16:17], v[0:1], 2, s[14:15]
	global_atomic_add v0, v[16:17], v53, off sc0
	s_and_b64 s[6:7], vcc, s[6:7]
	v_cndmask_b32_e64 v15, v15, v13, s[6:7]
	v_cndmask_b32_e32 v13, v13, v14, vcc
	v_sub_f32_e32 v13, v15, v13
	v_mul_f32_e32 v13, 0x3fb8aa3b, v13
	s_lshl_b32 s0, s24, 1
	v_exp_f32_e32 v13, v13
	s_ashr_i32 s1, s0, 31
	s_lshl_b64 s[10:11], s[0:1], 2
	s_add_u32 s6, s31, s10
	s_addc_u32 s7, s33, s11
	v_add_f32_e32 v14, 1.0, v13
	global_store_dwordx2 v1, v[10:11], s[6:7]
	v_div_scale_f32 v15, s[6:7], v14, v14, 1.0
	v_div_scale_f32 v17, s[6:7], v14, v14, v13
	v_rcp_f32_e32 v19, v15
	v_rcp_f32_e32 v20, v17
	s_or_b32 s0, s0, 1
	s_ashr_i32 s1, s0, 31
	v_fma_f32 v21, -v15, v19, 1.0
	s_add_u32 s12, s35, s10
	v_div_scale_f32 v16, vcc, 1.0, v14, 1.0
	v_fma_f32 v28, -v17, v20, 1.0
	v_fmac_f32_e32 v19, v21, v19
	s_addc_u32 s13, s36, s11
	s_lshl_b64 s[0:1], s[0:1], 2
	v_div_scale_f32 v18, s[6:7], v13, v14, v13
	v_fmac_f32_e32 v20, v28, v20
	v_mul_f32_e32 v21, v16, v19
	s_add_u32 s24, s35, s0
	v_mul_f32_e32 v28, v18, v20
	v_fma_f32 v29, -v15, v21, v16
	s_addc_u32 s25, s36, s1
	v_fma_f32 v30, -v17, v28, v18
	v_fmac_f32_e32 v21, v29, v19
	s_add_u32 s10, s37, s10
	v_fmac_f32_e32 v28, v30, v20
	v_fma_f32 v15, -v15, v21, v16
	s_addc_u32 s11, s38, s11
	v_fma_f32 v16, -v17, v28, v18
	v_div_fmas_f32 v15, v15, v19, v21
	s_mov_b64 vcc, s[6:7]
	s_add_u32 s0, s37, s0
	v_div_fixup_f32 v15, v15, v14, 1.0
	v_div_fmas_f32 v16, v16, v20, v28
	s_addc_u32 s1, s38, s1
	v_div_fixup_f32 v13, v16, v14, v13
	global_store_dword v1, v15, s[10:11]
	s_waitcnt vmcnt(3)
	global_store_dword v1, v12, s[12:13]
	s_waitcnt vmcnt(3)
	global_store_dword v1, v0, s[24:25]
	global_store_dword v1, v13, s[0:1]
	s_branch .LBB0_2067
